# speedup vs baseline: 1.0141x; 1.0141x over previous
_Z8pam_prepPKfS0_S0_S0_PDv4_jS2_S2_PfS3_:
	s_load_dwordx8 s[4:11], s[0:1], 0x0
	s_load_dwordx8 s[12:19], s[0:1], 0x20
	s_load_dwordx2 s[20:21], s[0:1], 0x40
	v_and_b32_e32 v1, 63, v0
	v_lshrrev_b32_e32 v4, 6, v0
	v_and_b32_e32 v2, 31, v1
	v_lshrrev_b32_e32 v3, 5, v1
	v_readfirstlane_b32 s22, v4
	v_lshlrev_b32_e32 v14, 4, v1
	s_mul_i32 s23, s2, 0x1900
	s_lshl_b32 s30, s2, 12
	s_lshl_b32 s31, s2, 10
	s_waitcnt lgkmcnt(0)
	s_add_u32 s24, s4, s23
	s_addc_u32 s25, s5, 0
	s_add_u32 s28, s16, s30
	s_addc_u32 s29, s17, 0
	s_cmp_ge_u32 s22, 2
	s_cbranch_scc1 .Lpp_tail
	v_mov_b32_e32 v40, 0
	v_mov_b32_e32 v41, 0
	v_mov_b32_e32 v42, 0
	v_mov_b32_e32 v43, 0
	v_mov_b32_e32 v44, 0
	v_mov_b32_e32 v45, 0
	v_mov_b32_e32 v46, 0
	v_mov_b32_e32 v47, 0
	v_mov_b32_e32 v48, 0
	v_mov_b32_e32 v49, 0
	v_mov_b32_e32 v50, 0
	v_mov_b32_e32 v51, 0
	v_mov_b32_e32 v52, 0
	v_mov_b32_e32 v53, 0
	v_mov_b32_e32 v54, 0
	v_mov_b32_e32 v55, 0
	v_mov_b32_e32 v56, 0
	v_mov_b32_e32 v57, 0
	v_mov_b32_e32 v58, 0
	v_mov_b32_e32 v59, 0
	v_mov_b32_e32 v60, 0
	v_mov_b32_e32 v61, 0
	v_mov_b32_e32 v62, 0
	v_mov_b32_e32 v63, 0
	v_mov_b32_e32 v64, 0
	v_mov_b32_e32 v65, 0
	v_mov_b32_e32 v66, 0
	v_mov_b32_e32 v67, 0
	v_mov_b32_e32 v68, 0
	v_mov_b32_e32 v69, 0
	v_mov_b32_e32 v70, 0
	v_mov_b32_e32 v71, 0
	v_mov_b32_e32 v72, 0
	v_mov_b32_e32 v73, 0
	v_mov_b32_e32 v74, 0
	v_mov_b32_e32 v75, 0
	v_mov_b32_e32 v76, 0
	v_mov_b32_e32 v77, 0
	v_mov_b32_e32 v78, 0
	v_mov_b32_e32 v79, 0
	v_mul_u32_u24_e32 v5, 0xc8, v2
	v_lshl_add_u32 v5, v3, 5, v5
	global_load_dwordx4 v[16:19], v5, s[24:25] offset:0
	global_load_dwordx4 v[20:23], v5, s[24:25] offset:16
	global_load_dwordx4 v[24:27], v5, s[24:25] offset:64
	global_load_dwordx4 v[28:31], v5, s[24:25] offset:80
	global_load_dwordx4 v[32:35], v5, s[24:25] offset:128
	global_load_dwordx4 v[36:39], v5, s[24:25] offset:144
	s_mov_b32 exec_hi, 0
	global_load_dwordx2 v[40:41], v5, s[24:25] offset:192
	s_mov_b64 exec, -1
	v_mul_u32_u24_e32 v6, 0x640, v3
	v_lshl_add_u32 v6, v2, 2, v6
	s_cmp_eq_u32 s22, 1
	s_cbranch_scc1 .Lpp_w1
	v_add_u32_e32 v7, 0xc80, v6
	v_add_u32_e32 v8, 0x1900, v6
	v_add_u32_e32 v9, 0x2580, v6
	global_load_dword v48, v6, s[10:11] offset:0
	global_load_dword v49, v6, s[10:11] offset:200
	global_load_dword v50, v6, s[10:11] offset:400
	global_load_dword v51, v6, s[10:11] offset:600
	global_load_dword v52, v6, s[10:11] offset:800
	global_load_dword v53, v6, s[10:11] offset:1000
	global_load_dword v54, v6, s[10:11] offset:1200
	global_load_dword v55, v6, s[10:11] offset:1400
	global_load_dword v56, v7, s[10:11] offset:0
	global_load_dword v57, v7, s[10:11] offset:200
	global_load_dword v58, v7, s[10:11] offset:400
	global_load_dword v59, v7, s[10:11] offset:600
	global_load_dword v60, v7, s[10:11] offset:800
	global_load_dword v61, v7, s[10:11] offset:1000
	global_load_dword v62, v7, s[10:11] offset:1200
	global_load_dword v63, v7, s[10:11] offset:1400
	global_load_dword v64, v8, s[10:11] offset:0
	global_load_dword v65, v8, s[10:11] offset:200
	global_load_dword v66, v8, s[10:11] offset:400
	global_load_dword v67, v8, s[10:11] offset:600
	global_load_dword v68, v8, s[10:11] offset:800
	global_load_dword v69, v8, s[10:11] offset:1000
	global_load_dword v70, v8, s[10:11] offset:1200
	global_load_dword v71, v8, s[10:11] offset:1400
	s_mov_b64 s[44:45], exec
	s_mov_b32 exec_hi, 0
	global_load_dword v72, v9, s[10:11] offset:0
	global_load_dword v73, v9, s[10:11] offset:200
	s_mov_b64 exec, s[44:45]
	s_waitcnt vmcnt(26)
	v_cvt_pk_f16_f32 v80, v16, v17
	v_cvt_pk_f16_f32 v81, v18, v19
	v_cvt_pk_f16_f32 v82, v20, v21
	v_cvt_pk_f16_f32 v83, v22, v23
	v_cvt_pk_f16_f32 v84, v24, v25
	v_cvt_pk_f16_f32 v85, v26, v27
	v_cvt_pk_f16_f32 v86, v28, v29
	v_cvt_pk_f16_f32 v87, v30, v31
	v_cvt_pk_f16_f32 v88, v32, v33
	v_cvt_pk_f16_f32 v89, v34, v35
	v_cvt_pk_f16_f32 v90, v36, v37
	v_cvt_pk_f16_f32 v91, v38, v39
	v_cvt_pk_f16_f32 v92, v40, v41
	v_cvt_pk_f16_f32 v93, v42, v43
	v_cvt_pk_f16_f32 v94, v44, v45
	v_cvt_pk_f16_f32 v95, v46, v47
	s_waitcnt vmcnt(0)
	v_cvt_pk_f16_f32 v112, v48, v49
	v_cvt_pk_f16_f32 v113, v50, v51
	v_cvt_pk_f16_f32 v114, v52, v53
	v_cvt_pk_f16_f32 v115, v54, v55
	v_cvt_pk_f16_f32 v116, v56, v57
	v_cvt_pk_f16_f32 v117, v58, v59
	v_cvt_pk_f16_f32 v118, v60, v61
	v_cvt_pk_f16_f32 v119, v62, v63
	v_cvt_pk_f16_f32 v120, v64, v65
	v_cvt_pk_f16_f32 v121, v66, v67
	v_cvt_pk_f16_f32 v122, v68, v69
	v_cvt_pk_f16_f32 v123, v70, v71
	v_cvt_pk_f16_f32 v124, v72, v73
	v_cvt_pk_f16_f32 v125, v74, v75
	v_cvt_pk_f16_f32 v126, v76, v77
	v_cvt_pk_f16_f32 v127, v78, v79
	s_nop 1
	v_mfma_f32_32x32x16_f16 v[144:159], v[80:83], v[112:115], 0
	v_mfma_f32_32x32x16_f16 v[144:159], v[84:87], v[116:119], v[144:159]
	v_mfma_f32_32x32x16_f16 v[144:159], v[88:91], v[120:123], v[144:159]
	v_mfma_f32_32x32x16_f16 v[144:159], v[92:95], v[124:127], v[144:159]
	s_mov_b32 s32, 0
	s_branch .Lpp_vstore
.Lpp_w1:
	v_add_u32_e32 v6, 0x80, v6
	v_add_u32_e32 v7, 0xc80, v6
	v_add_u32_e32 v8, 0x1900, v6
	v_add_u32_e32 v9, 0x2580, v6
	v_subrev_u32_e32 v10, 18, v2
	v_mul_u32_u24_e32 v11, 0xc0, v3
	v_lshl_add_u32 v11, v10, 2, v11
	v_subrev_u32_e32 v12, 24, v11
	s_mov_b32 exec_lo, 0x3ffff
	s_mov_b32 exec_hi, 0x3ffff
	global_load_dword v48, v6, s[10:11] offset:0
	global_load_dword v49, v6, s[10:11] offset:200
	global_load_dword v50, v6, s[10:11] offset:400
	global_load_dword v51, v6, s[10:11] offset:600
	global_load_dword v52, v6, s[10:11] offset:800
	global_load_dword v53, v6, s[10:11] offset:1000
	global_load_dword v54, v6, s[10:11] offset:1200
	global_load_dword v55, v6, s[10:11] offset:1400
	global_load_dword v56, v7, s[10:11] offset:0
	global_load_dword v57, v7, s[10:11] offset:200
	global_load_dword v58, v7, s[10:11] offset:400
	global_load_dword v59, v7, s[10:11] offset:600
	global_load_dword v60, v7, s[10:11] offset:800
	global_load_dword v61, v7, s[10:11] offset:1000
	global_load_dword v62, v7, s[10:11] offset:1200
	global_load_dword v63, v7, s[10:11] offset:1400
	global_load_dword v64, v8, s[10:11] offset:0
	global_load_dword v65, v8, s[10:11] offset:200
	global_load_dword v66, v8, s[10:11] offset:400
	global_load_dword v67, v8, s[10:11] offset:600
	global_load_dword v68, v8, s[10:11] offset:800
	global_load_dword v69, v8, s[10:11] offset:1000
	global_load_dword v70, v8, s[10:11] offset:1200
	global_load_dword v71, v8, s[10:11] offset:1400
	s_mov_b64 s[44:45], exec
	s_mov_b32 exec_hi, 0
	global_load_dword v72, v9, s[10:11] offset:0
	global_load_dword v73, v9, s[10:11] offset:200
	s_mov_b64 exec, s[44:45]
	s_mov_b32 exec_lo, 0xfc0000
	s_mov_b32 exec_hi, 0xfc0000
	global_load_dword v48, v11, s[6:7] offset:0
	global_load_dword v49, v11, s[6:7] offset:24
	global_load_dword v50, v11, s[6:7] offset:48
	global_load_dword v51, v11, s[6:7] offset:72
	global_load_dword v52, v11, s[6:7] offset:96
	global_load_dword v53, v11, s[6:7] offset:120
	global_load_dword v54, v11, s[6:7] offset:144
	global_load_dword v55, v11, s[6:7] offset:168
	global_load_dword v56, v11, s[6:7] offset:384
	global_load_dword v57, v11, s[6:7] offset:408
	global_load_dword v58, v11, s[6:7] offset:432
	global_load_dword v59, v11, s[6:7] offset:456
	global_load_dword v60, v11, s[6:7] offset:480
	global_load_dword v61, v11, s[6:7] offset:504
	global_load_dword v62, v11, s[6:7] offset:528
	global_load_dword v63, v11, s[6:7] offset:552
	global_load_dword v64, v11, s[6:7] offset:768
	global_load_dword v65, v11, s[6:7] offset:792
	global_load_dword v66, v11, s[6:7] offset:816
	global_load_dword v67, v11, s[6:7] offset:840
	global_load_dword v68, v11, s[6:7] offset:864
	global_load_dword v69, v11, s[6:7] offset:888
	global_load_dword v70, v11, s[6:7] offset:912
	global_load_dword v71, v11, s[6:7] offset:936
	s_mov_b64 s[44:45], exec
	s_mov_b32 exec_hi, 0
	global_load_dword v72, v11, s[6:7] offset:1152
	global_load_dword v73, v11, s[6:7] offset:1176
	s_mov_b64 exec, s[44:45]
	s_mov_b32 exec_lo, 0x3f000000
	s_mov_b32 exec_hi, 0x3f000000
	global_load_dword v48, v12, s[8:9] offset:0
	global_load_dword v49, v12, s[8:9] offset:24
	global_load_dword v50, v12, s[8:9] offset:48
	global_load_dword v51, v12, s[8:9] offset:72
	global_load_dword v52, v12, s[8:9] offset:96
	global_load_dword v53, v12, s[8:9] offset:120
	global_load_dword v54, v12, s[8:9] offset:144
	global_load_dword v55, v12, s[8:9] offset:168
	global_load_dword v56, v12, s[8:9] offset:384
	global_load_dword v57, v12, s[8:9] offset:408
	global_load_dword v58, v12, s[8:9] offset:432
	global_load_dword v59, v12, s[8:9] offset:456
	global_load_dword v60, v12, s[8:9] offset:480
	global_load_dword v61, v12, s[8:9] offset:504
	global_load_dword v62, v12, s[8:9] offset:528
	global_load_dword v63, v12, s[8:9] offset:552
	global_load_dword v64, v12, s[8:9] offset:768
	global_load_dword v65, v12, s[8:9] offset:792
	global_load_dword v66, v12, s[8:9] offset:816
	global_load_dword v67, v12, s[8:9] offset:840
	global_load_dword v68, v12, s[8:9] offset:864
	global_load_dword v69, v12, s[8:9] offset:888
	global_load_dword v70, v12, s[8:9] offset:912
	global_load_dword v71, v12, s[8:9] offset:936
	s_mov_b64 s[44:45], exec
	s_mov_b32 exec_hi, 0
	global_load_dword v72, v12, s[8:9] offset:1152
	global_load_dword v73, v12, s[8:9] offset:1176
	s_mov_b64 exec, s[44:45]
	s_mov_b64 exec, -1
	s_waitcnt vmcnt(63)
	v_cvt_pk_f16_f32 v80, v16, v17
	v_cvt_pk_f16_f32 v81, v18, v19
	v_cvt_pk_f16_f32 v82, v20, v21
	v_cvt_pk_f16_f32 v83, v22, v23
	v_cvt_pk_f16_f32 v84, v24, v25
	v_cvt_pk_f16_f32 v85, v26, v27
	v_cvt_pk_f16_f32 v86, v28, v29
	v_cvt_pk_f16_f32 v87, v30, v31
	v_cvt_pk_f16_f32 v88, v32, v33
	v_cvt_pk_f16_f32 v89, v34, v35
	v_cvt_pk_f16_f32 v90, v36, v37
	v_cvt_pk_f16_f32 v91, v38, v39
	v_cvt_pk_f16_f32 v92, v40, v41
	v_cvt_pk_f16_f32 v93, v42, v43
	v_cvt_pk_f16_f32 v94, v44, v45
	v_cvt_pk_f16_f32 v95, v46, v47
	v_cvt_f32_f16_e32 v160, v80
	v_cvt_f32_f16_sdwa v161, v80 dst_sel:DWORD dst_unused:UNUSED_PAD src0_sel:WORD_1
	v_sub_f32_e32 v160, v16, v160
	v_sub_f32_e32 v161, v17, v161
	v_cvt_pk_f16_f32 v96, v160, v161
	v_cvt_f32_f16_e32 v160, v81
	v_cvt_f32_f16_sdwa v161, v81 dst_sel:DWORD dst_unused:UNUSED_PAD src0_sel:WORD_1
	v_sub_f32_e32 v160, v18, v160
	v_sub_f32_e32 v161, v19, v161
	v_cvt_pk_f16_f32 v97, v160, v161
	v_cvt_f32_f16_e32 v160, v82
	v_cvt_f32_f16_sdwa v161, v82 dst_sel:DWORD dst_unused:UNUSED_PAD src0_sel:WORD_1
	v_sub_f32_e32 v160, v20, v160
	v_sub_f32_e32 v161, v21, v161
	v_cvt_pk_f16_f32 v98, v160, v161
	v_cvt_f32_f16_e32 v160, v83
	v_cvt_f32_f16_sdwa v161, v83 dst_sel:DWORD dst_unused:UNUSED_PAD src0_sel:WORD_1
	v_sub_f32_e32 v160, v22, v160
	v_sub_f32_e32 v161, v23, v161
	v_cvt_pk_f16_f32 v99, v160, v161
	v_cvt_f32_f16_e32 v160, v84
	v_cvt_f32_f16_sdwa v161, v84 dst_sel:DWORD dst_unused:UNUSED_PAD src0_sel:WORD_1
	v_sub_f32_e32 v160, v24, v160
	v_sub_f32_e32 v161, v25, v161
	v_cvt_pk_f16_f32 v100, v160, v161
	v_cvt_f32_f16_e32 v160, v85
	v_cvt_f32_f16_sdwa v161, v85 dst_sel:DWORD dst_unused:UNUSED_PAD src0_sel:WORD_1
	v_sub_f32_e32 v160, v26, v160
	v_sub_f32_e32 v161, v27, v161
	v_cvt_pk_f16_f32 v101, v160, v161
	v_cvt_f32_f16_e32 v160, v86
	v_cvt_f32_f16_sdwa v161, v86 dst_sel:DWORD dst_unused:UNUSED_PAD src0_sel:WORD_1
	v_sub_f32_e32 v160, v28, v160
	v_sub_f32_e32 v161, v29, v161
	v_cvt_pk_f16_f32 v102, v160, v161
	v_cvt_f32_f16_e32 v160, v87
	v_cvt_f32_f16_sdwa v161, v87 dst_sel:DWORD dst_unused:UNUSED_PAD src0_sel:WORD_1
	v_sub_f32_e32 v160, v30, v160
	v_sub_f32_e32 v161, v31, v161
	v_cvt_pk_f16_f32 v103, v160, v161
	v_cvt_f32_f16_e32 v160, v88
	v_cvt_f32_f16_sdwa v161, v88 dst_sel:DWORD dst_unused:UNUSED_PAD src0_sel:WORD_1
	v_sub_f32_e32 v160, v32, v160
	v_sub_f32_e32 v161, v33, v161
	v_cvt_pk_f16_f32 v104, v160, v161
	v_cvt_f32_f16_e32 v160, v89
	v_cvt_f32_f16_sdwa v161, v89 dst_sel:DWORD dst_unused:UNUSED_PAD src0_sel:WORD_1
	v_sub_f32_e32 v160, v34, v160
	v_sub_f32_e32 v161, v35, v161
	v_cvt_pk_f16_f32 v105, v160, v161
	v_cvt_f32_f16_e32 v160, v90
	v_cvt_f32_f16_sdwa v161, v90 dst_sel:DWORD dst_unused:UNUSED_PAD src0_sel:WORD_1
	v_sub_f32_e32 v160, v36, v160
	v_sub_f32_e32 v161, v37, v161
	v_cvt_pk_f16_f32 v106, v160, v161
	v_cvt_f32_f16_e32 v160, v91
	v_cvt_f32_f16_sdwa v161, v91 dst_sel:DWORD dst_unused:UNUSED_PAD src0_sel:WORD_1
	v_sub_f32_e32 v160, v38, v160
	v_sub_f32_e32 v161, v39, v161
	v_cvt_pk_f16_f32 v107, v160, v161
	v_cvt_f32_f16_e32 v160, v92
	v_cvt_f32_f16_sdwa v161, v92 dst_sel:DWORD dst_unused:UNUSED_PAD src0_sel:WORD_1
	v_sub_f32_e32 v160, v40, v160
	v_sub_f32_e32 v161, v41, v161
	v_cvt_pk_f16_f32 v108, v160, v161
	v_cvt_f32_f16_e32 v160, v93
	v_cvt_f32_f16_sdwa v161, v93 dst_sel:DWORD dst_unused:UNUSED_PAD src0_sel:WORD_1
	v_sub_f32_e32 v160, v42, v160
	v_sub_f32_e32 v161, v43, v161
	v_cvt_pk_f16_f32 v109, v160, v161
	v_cvt_f32_f16_e32 v160, v94
	v_cvt_f32_f16_sdwa v161, v94 dst_sel:DWORD dst_unused:UNUSED_PAD src0_sel:WORD_1
	v_sub_f32_e32 v160, v44, v160
	v_sub_f32_e32 v161, v45, v161
	v_cvt_pk_f16_f32 v110, v160, v161
	v_cvt_f32_f16_e32 v160, v95
	v_cvt_f32_f16_sdwa v161, v95 dst_sel:DWORD dst_unused:UNUSED_PAD src0_sel:WORD_1
	v_sub_f32_e32 v160, v46, v160
	v_sub_f32_e32 v161, v47, v161
	v_cvt_pk_f16_f32 v111, v160, v161
	s_waitcnt vmcnt(0)
	v_cvt_pk_f16_f32 v112, v48, v49
	v_cvt_pk_f16_f32 v113, v50, v51
	v_cvt_pk_f16_f32 v114, v52, v53
	v_cvt_pk_f16_f32 v115, v54, v55
	v_cvt_pk_f16_f32 v116, v56, v57
	v_cvt_pk_f16_f32 v117, v58, v59
	v_cvt_pk_f16_f32 v118, v60, v61
	v_cvt_pk_f16_f32 v119, v62, v63
	v_cvt_pk_f16_f32 v120, v64, v65
	v_cvt_pk_f16_f32 v121, v66, v67
	v_cvt_pk_f16_f32 v122, v68, v69
	v_cvt_pk_f16_f32 v123, v70, v71
	v_cvt_pk_f16_f32 v124, v72, v73
	v_cvt_pk_f16_f32 v125, v74, v75
	v_cvt_pk_f16_f32 v126, v76, v77
	v_cvt_pk_f16_f32 v127, v78, v79
	v_cvt_f32_f16_e32 v160, v112
	v_cvt_f32_f16_sdwa v161, v112 dst_sel:DWORD dst_unused:UNUSED_PAD src0_sel:WORD_1
	v_sub_f32_e32 v160, v48, v160
	v_sub_f32_e32 v161, v49, v161
	v_cvt_pk_f16_f32 v128, v160, v161
	v_cvt_f32_f16_e32 v160, v113
	v_cvt_f32_f16_sdwa v161, v113 dst_sel:DWORD dst_unused:UNUSED_PAD src0_sel:WORD_1
	v_sub_f32_e32 v160, v50, v160
	v_sub_f32_e32 v161, v51, v161
	v_cvt_pk_f16_f32 v129, v160, v161
	v_cvt_f32_f16_e32 v160, v114
	v_cvt_f32_f16_sdwa v161, v114 dst_sel:DWORD dst_unused:UNUSED_PAD src0_sel:WORD_1
	v_sub_f32_e32 v160, v52, v160
	v_sub_f32_e32 v161, v53, v161
	v_cvt_pk_f16_f32 v130, v160, v161
	v_cvt_f32_f16_e32 v160, v115
	v_cvt_f32_f16_sdwa v161, v115 dst_sel:DWORD dst_unused:UNUSED_PAD src0_sel:WORD_1
	v_sub_f32_e32 v160, v54, v160
	v_sub_f32_e32 v161, v55, v161
	v_cvt_pk_f16_f32 v131, v160, v161
	v_cvt_f32_f16_e32 v160, v116
	v_cvt_f32_f16_sdwa v161, v116 dst_sel:DWORD dst_unused:UNUSED_PAD src0_sel:WORD_1
	v_sub_f32_e32 v160, v56, v160
	v_sub_f32_e32 v161, v57, v161
	v_cvt_pk_f16_f32 v132, v160, v161
	v_cvt_f32_f16_e32 v160, v117
	v_cvt_f32_f16_sdwa v161, v117 dst_sel:DWORD dst_unused:UNUSED_PAD src0_sel:WORD_1
	v_sub_f32_e32 v160, v58, v160
	v_sub_f32_e32 v161, v59, v161
	v_cvt_pk_f16_f32 v133, v160, v161
	v_cvt_f32_f16_e32 v160, v118
	v_cvt_f32_f16_sdwa v161, v118 dst_sel:DWORD dst_unused:UNUSED_PAD src0_sel:WORD_1
	v_sub_f32_e32 v160, v60, v160
	v_sub_f32_e32 v161, v61, v161
	v_cvt_pk_f16_f32 v134, v160, v161
	v_cvt_f32_f16_e32 v160, v119
	v_cvt_f32_f16_sdwa v161, v119 dst_sel:DWORD dst_unused:UNUSED_PAD src0_sel:WORD_1
	v_sub_f32_e32 v160, v62, v160
	v_sub_f32_e32 v161, v63, v161
	v_cvt_pk_f16_f32 v135, v160, v161
	v_cvt_f32_f16_e32 v160, v120
	v_cvt_f32_f16_sdwa v161, v120 dst_sel:DWORD dst_unused:UNUSED_PAD src0_sel:WORD_1
	v_sub_f32_e32 v160, v64, v160
	v_sub_f32_e32 v161, v65, v161
	v_cvt_pk_f16_f32 v136, v160, v161
	v_cvt_f32_f16_e32 v160, v121
	v_cvt_f32_f16_sdwa v161, v121 dst_sel:DWORD dst_unused:UNUSED_PAD src0_sel:WORD_1
	v_sub_f32_e32 v160, v66, v160
	v_sub_f32_e32 v161, v67, v161
	v_cvt_pk_f16_f32 v137, v160, v161
	v_cvt_f32_f16_e32 v160, v122
	v_cvt_f32_f16_sdwa v161, v122 dst_sel:DWORD dst_unused:UNUSED_PAD src0_sel:WORD_1
	v_sub_f32_e32 v160, v68, v160
	v_sub_f32_e32 v161, v69, v161
	v_cvt_pk_f16_f32 v138, v160, v161
	v_cvt_f32_f16_e32 v160, v123
	v_cvt_f32_f16_sdwa v161, v123 dst_sel:DWORD dst_unused:UNUSED_PAD src0_sel:WORD_1
	v_sub_f32_e32 v160, v70, v160
	v_sub_f32_e32 v161, v71, v161
	v_cvt_pk_f16_f32 v139, v160, v161
	v_cvt_f32_f16_e32 v160, v124
	v_cvt_f32_f16_sdwa v161, v124 dst_sel:DWORD dst_unused:UNUSED_PAD src0_sel:WORD_1
	v_sub_f32_e32 v160, v72, v160
	v_sub_f32_e32 v161, v73, v161
	v_cvt_pk_f16_f32 v140, v160, v161
	v_cvt_f32_f16_e32 v160, v125
	v_cvt_f32_f16_sdwa v161, v125 dst_sel:DWORD dst_unused:UNUSED_PAD src0_sel:WORD_1
	v_sub_f32_e32 v160, v74, v160
	v_sub_f32_e32 v161, v75, v161
	v_cvt_pk_f16_f32 v141, v160, v161
	v_cvt_f32_f16_e32 v160, v126
	v_cvt_f32_f16_sdwa v161, v126 dst_sel:DWORD dst_unused:UNUSED_PAD src0_sel:WORD_1
	v_sub_f32_e32 v160, v76, v160
	v_sub_f32_e32 v161, v77, v161
	v_cvt_pk_f16_f32 v142, v160, v161
	v_cvt_f32_f16_e32 v160, v127
	v_cvt_f32_f16_sdwa v161, v127 dst_sel:DWORD dst_unused:UNUSED_PAD src0_sel:WORD_1
	v_sub_f32_e32 v160, v78, v160
	v_sub_f32_e32 v161, v79, v161
	v_cvt_pk_f16_f32 v143, v160, v161
	s_nop 1
	v_mfma_f32_32x32x16_f16 v[144:159], v[80:83], v[112:115], 0
	v_mfma_f32_32x32x16_f16 v[144:159], v[96:99], v[112:115], v[144:159]
	v_mfma_f32_32x32x16_f16 v[144:159], v[80:83], v[128:131], v[144:159]
	v_mfma_f32_32x32x16_f16 v[144:159], v[84:87], v[116:119], v[144:159]
	v_mfma_f32_32x32x16_f16 v[144:159], v[100:103], v[116:119], v[144:159]
	v_mfma_f32_32x32x16_f16 v[144:159], v[84:87], v[132:135], v[144:159]
	v_mfma_f32_32x32x16_f16 v[144:159], v[88:91], v[120:123], v[144:159]
	v_mfma_f32_32x32x16_f16 v[144:159], v[104:107], v[120:123], v[144:159]
	v_mfma_f32_32x32x16_f16 v[144:159], v[88:91], v[136:139], v[144:159]
	v_mfma_f32_32x32x16_f16 v[144:159], v[92:95], v[124:127], v[144:159]
	v_mfma_f32_32x32x16_f16 v[144:159], v[108:111], v[124:127], v[144:159]
	v_mfma_f32_32x32x16_f16 v[144:159], v[92:95], v[140:143], v[144:159]
	s_nop 15
	v_mul_u32_u24_e32 v13, 0xc0, v3
	v_lshl_add_u32 v13, v10, 2, v13
	s_mov_b32 exec_lo, 0x3ffc0000
	s_mov_b32 exec_hi, 0x3ffc0000
	ds_write_b32 v13, v144 offset:0
	ds_write_b32 v13, v145 offset:48
	ds_write_b32 v13, v146 offset:96
	ds_write_b32 v13, v147 offset:144
	ds_write_b32 v13, v148 offset:384
	ds_write_b32 v13, v149 offset:432
	ds_write_b32 v13, v150 offset:480
	ds_write_b32 v13, v151 offset:528
	ds_write_b32 v13, v152 offset:768
	ds_write_b32 v13, v153 offset:816
	ds_write_b32 v13, v154 offset:864
	ds_write_b32 v13, v155 offset:912
	ds_write_b32 v13, v156 offset:1152
	ds_write_b32 v13, v157 offset:1200
	ds_write_b32 v13, v158 offset:1248
	ds_write_b32 v13, v159 offset:1296
	s_mov_b64 exec, -1
	v_and_b32_e32 v160, 27, v2
	v_cmp_eq_u32_e32 vcc, 18, v160
	s_nop 1
	v_cndmask_b32_e64 v161, 0, 1.0, vcc
	v_cmp_lt_u32_e32 vcc, 17, v2
	s_nop 1
	v_cndmask_b32_e32 v144, v144, v161, vcc
	v_cndmask_b32_e32 v145, v145, v161, vcc
	v_cndmask_b32_e32 v146, v146, v161, vcc
	v_cndmask_b32_e32 v147, v147, v161, vcc
	v_cndmask_b32_e32 v148, v148, v161, vcc
	v_cndmask_b32_e32 v149, v149, v161, vcc
	v_cndmask_b32_e32 v150, v150, v161, vcc
	v_cndmask_b32_e32 v151, v151, v161, vcc
	v_cndmask_b32_e32 v152, v152, v161, vcc
	v_cndmask_b32_e32 v153, v153, v161, vcc
	v_cndmask_b32_e32 v154, v154, v161, vcc
	v_cndmask_b32_e32 v155, v155, v161, vcc
	v_cndmask_b32_e32 v156, v156, v161, vcc
	v_cndmask_b32_e32 v157, v157, v161, vcc
	v_cndmask_b32_e32 v158, v158, v161, vcc
	v_cndmask_b32_e32 v159, v159, v161, vcc
	s_movk_i32 s32, 0x800
.Lpp_vstore:
	s_nop 15
	s_add_u32 s34, s28, s32
	s_addc_u32 s35, s29, 0
	v_cvt_pk_bf16_f32 v164, v144, v145
	v_cvt_pk_bf16_f32 v165, v146, v147
	v_cvt_pk_bf16_f32 v166, v148, v149
	v_cvt_pk_bf16_f32 v167, v150, v151
	global_store_dwordx4 v14, v[164:167], s[34:35]
	s_nop 1
	v_cvt_pk_bf16_f32 v164, v152, v153
	v_cvt_pk_bf16_f32 v165, v154, v155
	v_cvt_pk_bf16_f32 v166, v156, v157
	v_cvt_pk_bf16_f32 v167, v158, v159
	global_store_dwordx4 v14, v[164:167], s[34:35] offset:1024
	s_nop 1
	s_waitcnt lgkmcnt(0)
	s_barrier
	s_endpgm
.Lpp_tail:
	v_mul_u32_u24_e32 v4, 48, v2
	v_cmp_gt_u32_e32 vcc, 32, v1
	s_barrier
	s_cmp_eq_u32 s22, 3
	s_cbranch_scc1 .Lpp_q
	ds_read_b64 v[16:17], v4 offset:24
	ds_read_b64 v[18:19], v4 offset:32
	ds_read_b64 v[20:21], v4 offset:40
	v_mov_b32_e32 v27, 0x3c00
	v_cndmask_b32_e32 v27, 0, v27, vcc
	s_add_u32 s34, s12, s31
	s_addc_u32 s35, s13, 0
	s_waitcnt lgkmcnt(0)
	v_cvt_pk_f16_f32 v24, v16, v17
	v_cvt_pk_f16_f32 v25, v18, v19
	v_cvt_pk_f16_f32 v26, v20, v21
	global_store_dwordx4 v14, v[24:27], s[34:35]
	v_fma_f32 v28, v16, v16, 0
	v_fmac_f32_e32 v28, v17, v17
	v_fmac_f32_e32 v28, v18, v18
	v_fmac_f32_e32 v28, v19, v19
	v_fmac_f32_e32 v28, v20, v20
	v_fmac_f32_e32 v28, v21, v21
	s_nop 1
	v_max_f32_dpp v28, v28, v28 quad_perm:[1,0,3,2] row_mask:0xf bank_mask:0xf
	s_nop 1
	v_max_f32_dpp v28, v28, v28 quad_perm:[2,3,0,1] row_mask:0xf bank_mask:0xf
	s_nop 1
	v_max_f32_dpp v28, v28, v28 row_half_mirror row_mask:0xf bank_mask:0xf
	s_nop 1
	v_max_f32_dpp v28, v28, v28 row_mirror row_mask:0xf bank_mask:0xf
	s_nop 1
	v_readlane_b32 s36, v28, 0
	v_readlane_b32 s37, v28, 16
	s_nop 2
	v_mov_b32_e32 v29, s36
	v_max_f32_e32 v29, s37, v29
	s_lshl_b32 s38, s2, 2
	s_add_u32 s34, s20, s38
	s_addc_u32 s35, s21, 0
	v_mov_b32_e32 v30, 0
	s_mov_b32 exec_lo, 1
	s_mov_b32 exec_hi, 0
	global_store_dword v30, v29, s[34:35]
	s_endpgm
.Lpp_q:
	ds_read_b64 v[16:17], v4 offset:0
	ds_read_b64 v[18:19], v4 offset:8
	ds_read_b64 v[20:21], v4 offset:16
	s_mov_b32 s23, 0x3fb8aa3b
	s_add_u32 s34, s14, s31
	s_addc_u32 s35, s15, 0
	s_waitcnt lgkmcnt(0)
	v_fma_mixlo_f16 v32, v16, s23, 0
	v_fma_mixlo_f16 v40, v16, s23, -v32 op_sel_hi:[0,0,1]
	v_cndmask_b32_e32 v48, v40, v32, vcc
	v_fma_mixlo_f16 v33, v17, s23, 0
	v_fma_mixlo_f16 v41, v17, s23, -v33 op_sel_hi:[0,0,1]
	v_cndmask_b32_e32 v49, v41, v33, vcc
	v_fma_mixlo_f16 v34, v18, s23, 0
	v_fma_mixlo_f16 v42, v18, s23, -v34 op_sel_hi:[0,0,1]
	v_cndmask_b32_e32 v50, v42, v34, vcc
	v_fma_mixlo_f16 v35, v19, s23, 0
	v_fma_mixlo_f16 v43, v19, s23, -v35 op_sel_hi:[0,0,1]
	v_cndmask_b32_e32 v51, v43, v35, vcc
	v_fma_mixlo_f16 v36, v20, s23, 0
	v_fma_mixlo_f16 v44, v20, s23, -v36 op_sel_hi:[0,0,1]
	v_cndmask_b32_e32 v52, v44, v36, vcc
	v_fma_mixlo_f16 v37, v21, s23, 0
	v_fma_mixlo_f16 v45, v21, s23, -v37 op_sel_hi:[0,0,1]
	v_cndmask_b32_e32 v53, v45, v37, vcc
	v_mov_b32_e32 v31, 0xfb53
	v_cndmask_b32_e32 v31, 0, v31, vcc
	v_pack_b32_f16 v24, v48, v49
	v_pack_b32_f16 v25, v50, v51
	v_pack_b32_f16 v26, v52, v53
	v_pack_b32_f16 v27, 0, v31
	global_store_dwordx4 v14, v[24:27], s[34:35]
	s_mov_b32 exec_hi, 0
	v_mul_f32_e32 v16, 0x3fb8aa3b, v16
	v_mul_f32_e32 v17, 0x3fb8aa3b, v17
	v_mul_f32_e32 v18, 0x3fb8aa3b, v18
	v_mul_f32_e32 v19, 0x3fb8aa3b, v19
	v_mul_f32_e32 v20, 0x3fb8aa3b, v20
	v_mul_f32_e32 v21, 0x3fb8aa3b, v21
	v_fma_f32 v16, v16, v16, 0
	v_fmac_f32_e32 v16, v17, v17
	v_fmac_f32_e32 v16, v18, v18
	v_fmac_f32_e32 v16, v19, v19
	v_fmac_f32_e32 v16, v20, v20
	v_fmac_f32_e32 v16, v21, v21
	s_mov_b32 s36, 0xf800000
	v_mul_f32_e32 v17, 0x4f800000, v16
	v_cmp_gt_f32_e32 vcc, s36, v16
	s_nop 1
	v_cndmask_b32_e32 v16, v16, v17, vcc
	v_sqrt_f32_e32 v17, v16
	s_nop 0
	v_add_u32_e32 v18, -1, v17
	v_fma_f32 v19, -v18, v17, v16
	v_cmp_ge_f32_e64 s[36:37], 0, v19
	v_add_u32_e32 v19, 1, v17
	s_nop 0
	v_cndmask_b32_e64 v18, v17, v18, s[36:37]
	v_fma_f32 v17, -v19, v17, v16
	v_cmp_lt_f32_e64 s[36:37], 0, v17
	s_nop 1
	v_cndmask_b32_e64 v17, v18, v19, s[36:37]
	v_mul_f32_e32 v18, 0x37800000, v17
	v_cndmask_b32_e32 v17, v17, v18, vcc
	v_mov_b32_e32 v18, 0x260
	v_cmp_class_f32_e32 vcc, v16, v18
	s_nop 1
	v_cndmask_b32_e32 v18, v17, v16, vcc
	s_lshl_b32 s38, s2, 7
	s_add_u32 s34, s18, s38
	s_addc_u32 s35, s19, 0
	v_lshlrev_b32_e32 v30, 2, v2
	global_store_dword v30, v18, s[34:35]
	s_endpgm

	.amdhsa_kernel _Z8pam_prepPKfS0_S0_S0_PDv4_jS2_S2_PfS3_
		.amdhsa_group_segment_fixed_size 29184
		.amdhsa_private_segment_fixed_size 0
		.amdhsa_kernarg_size 72
		.amdhsa_user_sgpr_count 2
		.amdhsa_user_sgpr_dispatch_ptr 0
		.amdhsa_user_sgpr_queue_ptr 0
		.amdhsa_user_sgpr_kernarg_segment_ptr 1
		.amdhsa_user_sgpr_dispatch_id 0
		.amdhsa_user_sgpr_kernarg_preload_length 0
		.amdhsa_user_sgpr_kernarg_preload_offset 0
		.amdhsa_user_sgpr_private_segment_size 0
		.amdhsa_uses_dynamic_stack 0
		.amdhsa_enable_private_segment 0
		.amdhsa_system_sgpr_workgroup_id_x 1
		.amdhsa_system_sgpr_workgroup_id_y 0
		.amdhsa_system_sgpr_workgroup_id_z 0
		.amdhsa_system_sgpr_workgroup_info 0
		.amdhsa_system_vgpr_workitem_id 0
		.amdhsa_next_free_vgpr 168
		.amdhsa_next_free_sgpr 96
		.amdhsa_accum_offset 168
		.amdhsa_reserve_vcc 1
		.amdhsa_float_round_mode_32 0
		.amdhsa_float_round_mode_16_64 0
		.amdhsa_float_denorm_mode_32 3
		.amdhsa_float_denorm_mode_16_64 3
		.amdhsa_dx10_clamp 1
		.amdhsa_ieee_mode 1
		.amdhsa_fp16_overflow 0
		.amdhsa_tg_split 0
		.amdhsa_exception_fp_ieee_invalid_op 0
		.amdhsa_exception_fp_denorm_src 0
		.amdhsa_exception_fp_ieee_div_zero 0
		.amdhsa_exception_fp_ieee_overflow 0
		.amdhsa_exception_fp_ieee_underflow 0
		.amdhsa_exception_fp_ieee_inexact 0
		.amdhsa_exception_int_div_zero 0
	.end_amdhsa_kernel

amdhsa.kernels:
  - .agpr_count:     0
    .args:
      - .actual_access:  read_only
        .address_space:  global
        .offset:         0
        .size:           8
        .value_kind:     global_buffer
      - .actual_access:  read_only
        .address_space:  global
        .offset:         8
        .size:           8
        .value_kind:     global_buffer
      - .actual_access:  read_only
        .address_space:  global
        .offset:         16
        .size:           8
        .value_kind:     global_buffer
      - .actual_access:  read_only
        .address_space:  global
        .offset:         24
        .size:           8
        .value_kind:     global_buffer
      - .actual_access:  write_only
        .address_space:  global
        .offset:         32
        .size:           8
        .value_kind:     global_buffer
      - .actual_access:  write_only
        .address_space:  global
        .offset:         40
        .size:           8
        .value_kind:     global_buffer
      - .actual_access:  write_only
        .address_space:  global
        .offset:         48
        .size:           8
        .value_kind:     global_buffer
      - .actual_access:  write_only
        .address_space:  global
        .offset:         56
        .size:           8
        .value_kind:     global_buffer
      - .actual_access:  write_only
        .address_space:  global
        .offset:         64
        .size:           8
        .value_kind:     global_buffer
    .group_segment_fixed_size: 29184
    .kernarg_segment_align: 8
    .kernarg_segment_size: 72
    .language:       OpenCL C
    .language_version:
      - 2
      - 0
    .max_flat_workgroup_size: 256
    .name:           _Z8pam_prepPKfS0_S0_S0_PDv4_jS2_S2_PfS3_
    .private_segment_fixed_size: 0
    .sgpr_count:     28
    .sgpr_spill_count: 0
    .symbol:         _Z8pam_prepPKfS0_S0_S0_PDv4_jS2_S2_PfS3_.kd
    .uniform_work_group_size: 1
    .uses_dynamic_stack: false
    .vgpr_count:     168
    .vgpr_spill_count: 0
    .wavefront_size: 64
  - .agpr_count:     0
    .args:
      - .address_space:  global
        .offset:         0
        .size:           8
        .value_kind:     global_buffer
      - .actual_access:  read_only
        .address_space:  global
        .offset:         8
        .size:           8
        .value_kind:     global_buffer
      - .address_space:  global
        .offset:         16
        .size:           8
        .value_kind:     global_buffer
      - .actual_access:  read_only
        .address_space:  global
        .offset:         24
        .size:           8
        .value_kind:     global_buffer
      - .actual_access:  read_only
        .address_space:  global
        .offset:         32
        .size:           8
        .value_kind:     global_buffer
      - .actual_access:  write_only
        .address_space:  global
        .offset:         40
        .size:           8
        .value_kind:     global_buffer
      - .actual_access:  write_only
        .address_space:  global
        .offset:         48
        .size:           8
        .value_kind:     global_buffer
    .group_segment_fixed_size: 133120
    .kernarg_segment_align: 8
    .kernarg_segment_size: 56
    .language:       OpenCL C
    .language_version:
      - 2
      - 0
    .max_flat_workgroup_size: 768
    .name:           _Z8pam_mainPKDv4_jS1_S1_PKfS3_PDF16_Pf
    .private_segment_fixed_size: 0
    .sgpr_count:     52
    .sgpr_spill_count: 0
    .symbol:         _Z8pam_mainPKDv4_jS1_S1_PKfS3_PDF16_Pf.kd
    .uniform_work_group_size: 1
    .uses_dynamic_stack: false
    .vgpr_count:     152
    .vgpr_spill_count: 0
    .wavefront_size: 64
  - .agpr_count:     0
    .args:
      - .actual_access:  read_only
        .address_space:  global
        .offset:         0
        .size:           8
        .value_kind:     global_buffer
      - .actual_access:  read_only
        .address_space:  global
        .offset:         8
        .size:           8
        .value_kind:     global_buffer
      - .actual_access:  read_only
        .address_space:  global
        .offset:         16
        .size:           8
        .value_kind:     global_buffer
      - .actual_access:  read_only
        .address_space:  global
        .offset:         24
        .size:           8
        .value_kind:     global_buffer
      - .actual_access:  write_only
        .address_space:  global
        .offset:         32
        .size:           8
        .value_kind:     global_buffer
    .group_segment_fixed_size: 0
    .kernarg_segment_align: 8
    .kernarg_segment_size: 40
    .language:       OpenCL C
    .language_version:
      - 2
      - 0
    .max_flat_workgroup_size: 256
    .name:           _Z11pam_combinePKDF16_PKfS2_S2_Pf
    .private_segment_fixed_size: 0
    .sgpr_count:     30
    .sgpr_spill_count: 0
    .symbol:         _Z11pam_combinePKDF16_PKfS2_S2_Pf.kd
    .uniform_work_group_size: 1
    .uses_dynamic_stack: false
    .vgpr_count:     84
    .vgpr_spill_count: 0
    .wavefront_size: 64
